# counted waits in the attention pass prologues: K(1) tile loads issued together with the Q/K(0)/V(0) loads, each LDS write waits only for its own data
# baseline (speedup 1.0000x reference)
; #define HLOADV(kt) do { const char* vb_ = (const char*)Vh + (size_t)(kt) * (64 * LDK * 2); sv0 = *(const bf16x8*)(vb_ + koff0); sv1 = *(const bf16x8*)(vb_ + koff1); } while (0)
; #define HLOADK(kt) do { const char* kb_ = (const char*)Kh + (size_t)(kt) * (64 * LDK * 2); sk0 = *(const bf16x8*)(kb_ + koff0); sk1 = *(const bf16x8*)(kb_ + koff1); } while (0)
; #define HWRITEV(b) do { char* d_ = V_lds + (b) * G16_V; *(bf16x8*)(d_ + vst0) = sv0; *(bf16x8*)(d_ + vst1) = sv1; } while (0)
; #define HWRITEK(b) do { char* d_ = K_lds + (b) * GB_K; *(bf16x8*)(d_ + KSWZ(sr, sc * 2)) = sk0; *(bf16x8*)(d_ + KSWZ(32 + sr, sc * 2)) = sk1; } while (0)
; #define HEXP() do { _Pragma("unroll") for (int kt = 0; kt < 4; ++kt) { _Pragma("unroll") for (int qt = 0; qt < 2; ++qt) { _Pragma("unroll") for (int i = 0; i < 4; ++i) s[kt][qt][i] = __builtin_amdgcn_exp2f(fmaf(s[kt][qt][i], C, mnC)); } } } while (0)
; template <int LDQ, int LDK, int LDO>
; __device__ __forceinline__ void attn_gqa16_body(const bf16* __restrict__ Qb, const bf16* __restrict__ Kh, const bf16* __restrict__ Vh, bf16* __restrict__ Ob, int seq, char* lds, float mref) {
;     ...
;   { int l16q = l16, gq = g, widq = wid; asm volatile("" : "+v"(l16q), "+v"(gq), "+v"(widq));
;     const bf16* Qw = Qb + (widq >> 2) * 128 + (long)((widq & 3) * QBLK + l16q) * LDQ + gq * 8;
; #pragma unroll
;     for (int qt = 0; qt < 2; ++qt)
; #pragma unroll
;       for (int ds = 0; ds < 4; ++ds) qr[qt][ds] = *reinterpret_cast<const bf16x8*>(Qw + (long)qt * 16 * LDQ + ds * 32); }
;   const int sr = tid >> 4, sc = (tid & 15) * 8;
;   const int vst0 = (sc >> 4) * VP16 + sr * 32 + ((sc >> 3) & 1) * 16, vst1 = vst0 + 1024;
;   const int vb0 = (int)(uintptr_t)V_lds + (4 * g + (l16 >> 2)) * 32 + (l16 & 3) * 8;
;   const int kb0 = l16 * 272 + g * 16;
;   bf16x8 sv0, sv1, sk0, sk1;
;   const unsigned koff0 = (unsigned)(sr * LDK + sc) * 2u, koff1 = koff0 + 32u * LDK * 2u;
;     ...
;   f32x4a s[4][2]; bf16x8 pb[2][2];
;     ...
;   const int NT = seq / KVBLK;
;   HLOADK(0); HLOADV(0); asm volatile("s_waitcnt vmcnt(0)" ::: "memory"); HWRITEK(0); HWRITEV(0);
;   HLOADK(1); asm volatile("s_waitcnt vmcnt(0)" ::: "memory"); HWRITEK(1); __syncthreads();
;   HLOADK(2); HLOADV(1);
;   HQK(0); HEXP();
.LBB0_646:
	s_and_b64 vcc, exec, s[14:15]
	s_cbranch_vccz .LBB0_641
	s_lshl_b32 s8, s45, 7
	s_and_b32 s8, s8, 0x3f80
	s_ashr_i32 s14, s45, 8
	s_mul_i32 s12, s8, 0x2400
	s_add_u32 s15, s33, s12
	s_addc_u32 s17, s35, 0
	s_lshl_b32 s13, s45, 1
	s_lshl_b32 s12, s14, 9
	s_and_b32 s13, s13, 0x100
	s_or_b32 s12, s12, s13
	s_ashr_i32 s13, s12, 31
	v_mov_b32_e32 v4, v180
	v_mov_b32_e32 v2, v185
	v_mov_b32_e32 v5, v176
	s_lshl_b64 s[12:13], s[12:13], 1
	s_add_u32 s16, s15, s12
	v_lshlrev_b32_e32 v6, 5, v2
	v_and_b32_e32 v2, 0xffffff80, v6
	s_addc_u32 s17, s17, s13
	v_ashrrev_i32_e32 v3, 31, v2
	v_and_b32_e32 v6, 0x60, v6
	s_lshl_b32 s14, s14, 7
	v_lshl_add_u64 v[2:3], v[2:3], 1, s[16:17]
	v_add_u32_e32 v4, v6, v4
	s_ashr_i32 s15, s14, 31
	v_mad_i64_i32 v[2:3], s[16:17], v4, s26, v[2:3]
	v_lshlrev_b32_e32 v4, 3, v5
	s_lshl_b64 s[46:47], s[14:15], 1
	v_ashrrev_i32_e32 v5, 31, v4
	s_add_u32 s48, s21, s46
	v_lshl_add_u64 v[6:7], v[4:5], 1, v[2:3]
	s_addc_u32 s49, s22, s47
	global_load_dwordx4 v[30:33], v[6:7], off
	global_load_dwordx4 v[18:21], v[6:7], off offset:64
	global_load_dwordx4 v[10:13], v[6:7], off offset:128
	global_load_dwordx4 v[2:5], v[6:7], off offset:192
	v_add_co_u32_e32 v6, vcc, s27, v6
	s_add_u32 s46, s23, s46
	s_nop 0
	v_addc_co_u32_e32 v7, vcc, 0, v7, vcc
	v_lshl_add_u64 v[102:103], s[48:49], 0, v[178:179]
	s_addc_u32 s47, s24, s47
	s_add_u32 s74, s46, 0x90000
	s_addc_u32 s75, s47, 0
	s_add_u32 s76, s74, 0x48000
	s_addc_u32 s77, s75, 0
	v_add_co_u32_e32 v34, vcc, s28, v102
	v_lshl_add_u64 v[104:105], s[46:47], 0, v[178:179]
	s_nop 0
	v_addc_co_u32_e32 v35, vcc, 0, v103, vcc
	v_add_co_u32_e32 v46, vcc, s28, v104
	global_load_dwordx4 v[38:41], v[6:7], off
	global_load_dwordx4 v[22:25], v[6:7], off offset:64
	global_load_dwordx4 v[14:17], v[6:7], off offset:128
	s_nop 0
	global_load_dwordx4 v[6:9], v[6:7], off offset:192
	v_addc_co_u32_e32 v47, vcc, 0, v105, vcc
	v_add_co_u32_e32 v50, vcc, s29, v102
	global_load_dwordx4 v[26:29], v[102:103], off
	s_nop 0
	global_load_dwordx4 v[34:37], v[34:35], off
	v_addc_co_u32_e32 v51, vcc, 0, v103, vcc
	v_add_co_u32_e32 v54, vcc, s30, v102
	global_load_dwordx4 v[42:45], v[104:105], off
	s_nop 0
	global_load_dwordx4 v[46:49], v[46:47], off
	v_addc_co_u32_e32 v55, vcc, 0, v103, vcc
	global_load_dwordx4 v[50:53], v[50:51], off
	s_nop 0
	global_load_dwordx4 v[54:57], v[54:55], off
	s_waitcnt vmcnt(5)
	ds_write_b128 v194, v[26:29] offset:33280
	s_waitcnt vmcnt(4)
	ds_write_b128 v194, v[34:37] offset:41984
	s_waitcnt vmcnt(3)
	ds_write_b128 v181, v[42:45]
	s_waitcnt vmcnt(2)
	ds_write_b128 v181, v[46:49] offset:1024
	s_waitcnt vmcnt(0)
	s_waitcnt vmcnt(1)
	ds_write_b128 v194, v[50:53] offset:50688
	s_waitcnt vmcnt(0)
	ds_write_b128 v194, v[54:57] offset:59392
	s_waitcnt lgkmcnt(0)
	s_barrier
	ds_read_b128 v[26:29], v182 offset:33280
	ds_read_b128 v[34:37], v182 offset:33344
	ds_read_b128 v[46:49], v182 offset:37632
	ds_read_b128 v[50:53], v182 offset:37696
	ds_read_b128 v[58:61], v182 offset:41984
	ds_read_b128 v[62:65], v182 offset:42048
	ds_read_b128 v[70:73], v182 offset:46336
	ds_read_b128 v[74:77], v182 offset:46400
	s_waitcnt lgkmcnt(7)
	v_mfma_f32_16x16x32_bf16 v[42:45], v[26:29], v[30:33], 0
	v_mfma_f32_16x16x32_bf16 v[26:29], v[26:29], v[38:41], 0
	s_waitcnt lgkmcnt(5)
	v_mfma_f32_16x16x32_bf16 v[54:57], v[46:49], v[30:33], 0
	v_mfma_f32_16x16x32_bf16 v[46:49], v[46:49], v[38:41], 0
	s_waitcnt lgkmcnt(3)
	v_mfma_f32_16x16x32_bf16 v[66:69], v[58:61], v[30:33], 0
	v_mfma_f32_16x16x32_bf16 v[58:61], v[58:61], v[38:41], 0
	s_waitcnt lgkmcnt(1)
	v_mfma_f32_16x16x32_bf16 v[78:81], v[70:73], v[30:33], 0
	v_mfma_f32_16x16x32_bf16 v[70:73], v[70:73], v[38:41], 0
	v_mfma_f32_16x16x32_bf16 v[42:45], v[34:37], v[18:21], v[42:45]
	v_mfma_f32_16x16x32_bf16 v[26:29], v[34:37], v[22:25], v[26:29]
	v_mfma_f32_16x16x32_bf16 v[34:37], v[50:53], v[18:21], v[54:57]
	v_mfma_f32_16x16x32_bf16 v[46:49], v[50:53], v[22:25], v[46:49]
	v_mfma_f32_16x16x32_bf16 v[50:53], v[62:65], v[18:21], v[66:69]
	v_mfma_f32_16x16x32_bf16 v[54:57], v[62:65], v[22:25], v[58:61]
	s_waitcnt lgkmcnt(0)
	v_mfma_f32_16x16x32_bf16 v[58:61], v[74:77], v[18:21], v[78:81]
	v_mfma_f32_16x16x32_bf16 v[62:65], v[74:77], v[22:25], v[70:73]
	ds_read_b128 v[66:69], v182 offset:33408
	ds_read_b128 v[74:77], v182 offset:33472
	s_waitcnt lgkmcnt(1)
	v_mfma_f32_16x16x32_bf16 v[42:45], v[66:69], v[10:13], v[42:45]
	v_mfma_f32_16x16x32_bf16 v[26:29], v[66:69], v[14:17], v[26:29]
	ds_read_b128 v[66:69], v182 offset:37760
	ds_read_b128 v[78:81], v182 offset:37824
	s_waitcnt lgkmcnt(1)
	v_mfma_f32_16x16x32_bf16 v[34:37], v[66:69], v[10:13], v[34:37]
	v_mfma_f32_16x16x32_bf16 v[46:49], v[66:69], v[14:17], v[46:49]
	ds_read_b128 v[66:69], v182 offset:42112
	ds_read_b128 v[82:85], v182 offset:42176
	s_waitcnt lgkmcnt(1)
	v_mfma_f32_16x16x32_bf16 v[50:53], v[66:69], v[10:13], v[50:53]
	v_mfma_f32_16x16x32_bf16 v[86:89], v[66:69], v[14:17], v[54:57]
	s_nop 2
	ds_read_b128 v[54:57], v182 offset:46464
	ds_read_b128 v[90:93], v182 offset:46528
	v_mfma_f32_16x16x32_bf16 v[66:69], v[74:77], v[6:9], v[26:29]
	s_nop 2
	v_add_co_u32_e32 v26, vcc, s25, v102
	s_waitcnt lgkmcnt(1)
; #define HLOADV(kt) do { const char* vb_ = (const char*)Vh + (size_t)(kt) * (64 * LDK * 2); sv0 = *(const bf16x8*)(vb_ + koff0); sv1 = *(const bf16x8*)(vb_ + koff1); } while (0)
; #define HLOADK(kt) do { const char* kb_ = (const char*)Kh + (size_t)(kt) * (64 * LDK * 2); sk0 = *(const bf16x8*)(kb_ + koff0); sk1 = *(const bf16x8*)(kb_ + koff1); } while (0)
; #define HEXP() do { _Pragma("unroll") for (int kt = 0; kt < 4; ++kt) { _Pragma("unroll") for (int qt = 0; qt < 2; ++qt) { _Pragma("unroll") for (int i = 0; i < 4; ++i) s[kt][qt][i] = __builtin_amdgcn_exp2f(fmaf(s[kt][qt][i], C, mnC)); } } } while (0)
; template <int LDQ, int LDK, int LDO>
; __device__ __forceinline__ void attn_gqa16_body(const bf16* __restrict__ Qb, const bf16* __restrict__ Kh, const bf16* __restrict__ Vh, bf16* __restrict__ Ob, int seq, char* lds, float mref) {
;     ...
;   HLOADK(2); HLOADV(1);
;   HQK(0); HEXP();
;   if (wid >= 4) __builtin_amdgcn_s_setprio(1);
;   for (int t = 0; t < NT; ++t) {
	v_mfma_f32_16x16x32_bf16 v[98:101], v[54:57], v[14:17], v[62:65]
	v_addc_co_u32_e32 v27, vcc, 0, v103, vcc
	v_add_co_u32_e32 v28, vcc, s31, v102
	v_mfma_f32_16x16x32_bf16 v[62:65], v[78:81], v[2:5], v[34:37]
	s_nop 0
	v_addc_co_u32_e32 v29, vcc, 0, v103, vcc
	global_load_dwordx4 v[106:109], v[26:27], off
	global_load_dwordx4 v[110:113], v[28:29], off
	v_add_co_u32_e32 v26, vcc, s29, v104
	v_mfma_f32_16x16x32_bf16 v[94:97], v[54:57], v[10:13], v[58:61]
	s_nop 0
	v_addc_co_u32_e32 v27, vcc, 0, v105, vcc
	v_add_co_u32_e32 v34, vcc, s30, v104
	v_mfma_f32_16x16x32_bf16 v[70:73], v[74:77], v[2:5], v[42:45]
	s_nop 0
	v_addc_co_u32_e32 v35, vcc, 0, v105, vcc
	s_nop 0
	v_mfma_f32_16x16x32_bf16 v[58:61], v[78:81], v[6:9], v[46:49]
	v_mfma_f32_16x16x32_bf16 v[54:57], v[82:85], v[2:5], v[50:53]
	v_mfma_f32_16x16x32_bf16 v[50:53], v[82:85], v[6:9], v[86:89]
	s_waitcnt lgkmcnt(0)
	v_mfma_f32_16x16x32_bf16 v[46:49], v[90:93], v[2:5], v[94:97]
	v_mfma_f32_16x16x32_bf16 v[42:45], v[90:93], v[6:9], v[98:101]
	s_and_saveexec_b64 s[16:17], s[4:5]
	s_setprio 1
	s_or_b64 exec, exec, s[16:17]
	v_add_f32_e32 v70, v186, v70
	v_add_f32_e32 v66, v186, v66
	v_add_f32_e32 v62, v186, v62
	v_add_f32_e32 v58, v186, v58
	v_add_f32_e32 v54, v186, v54
	v_add_f32_e32 v50, v186, v50
	v_add_f32_e32 v46, v186, v46
	v_add_f32_e32 v42, v186, v42
	v_exp_f32_e32 v158, v70
	v_add_f32_e32 v70, v186, v71
	v_exp_f32_e32 v159, v66
	v_add_f32_e32 v66, v186, v67
	v_exp_f32_e32 v168, v62
	v_add_f32_e32 v62, v186, v63
	v_exp_f32_e32 v169, v58
	v_add_f32_e32 v58, v186, v59
	v_exp_f32_e32 v142, v54
	v_add_f32_e32 v54, v186, v55
	v_exp_f32_e32 v143, v50
	v_add_f32_e32 v50, v186, v51
	v_exp_f32_e32 v134, v46
	v_add_f32_e32 v46, v186, v47
	v_exp_f32_e32 v135, v42
	v_add_f32_e32 v42, v186, v43
	v_exp_f32_e32 v152, v70
	v_add_f32_e32 v70, v186, v72
	v_exp_f32_e32 v153, v66
	v_add_f32_e32 v66, v186, v68
	v_exp_f32_e32 v170, v62
	v_add_f32_e32 v62, v186, v64
	v_exp_f32_e32 v171, v58
	v_add_f32_e32 v58, v186, v60
	v_exp_f32_e32 v172, v54
	v_add_f32_e32 v54, v186, v56
	v_exp_f32_e32 v173, v50
	v_add_f32_e32 v50, v186, v52
	v_exp_f32_e32 v138, v46
	v_add_f32_e32 v46, v186, v48
	v_exp_f32_e32 v139, v42
	v_add_f32_e32 v42, v186, v44
	v_exp_f32_e32 v156, v70
	v_add_f32_e32 v70, v186, v73
	v_exp_f32_e32 v157, v66
	v_add_f32_e32 v66, v186, v69
	v_exp_f32_e32 v164, v62
	v_add_f32_e32 v62, v186, v65
	v_exp_f32_e32 v165, v58
	v_add_f32_e32 v58, v186, v61
	v_exp_f32_e32 v144, v54
	v_add_f32_e32 v54, v186, v57
	v_exp_f32_e32 v145, v50
	v_add_f32_e32 v50, v186, v53
	v_exp_f32_e32 v136, v46
	v_add_f32_e32 v46, v186, v49
	v_exp_f32_e32 v137, v42
	v_add_f32_e32 v42, v186, v45
	v_exp_f32_e32 v160, v70
	v_exp_f32_e32 v161, v66
	v_exp_f32_e32 v166, v62
	v_exp_f32_e32 v167, v58
	v_exp_f32_e32 v174, v54
	v_exp_f32_e32 v175, v50
	v_exp_f32_e32 v140, v46
	v_exp_f32_e32 v141, v42
	v_mov_b32_e32 v50, 0
	v_lshl_add_u64 v[162:163], s[14:15], 1, v[154:155]
	s_mov_b32 s16, 0
	s_mov_b64 s[14:15], 0
	v_mov_b32_e32 v51, v50
	v_mov_b32_e32 v52, v50
	v_mov_b32_e32 v53, v50
	v_mov_b32_e32 v78, v50
	v_mov_b32_e32 v79, v50
	v_mov_b32_e32 v80, v50
	v_mov_b32_e32 v81, v50
	v_mov_b32_e32 v90, v50
	v_mov_b32_e32 v91, v50
	v_mov_b32_e32 v92, v50
	v_mov_b32_e32 v93, v50
	v_mov_b32_e32 v94, v50
	v_mov_b32_e32 v95, v50
	v_mov_b32_e32 v96, v50
	v_mov_b32_e32 v97, v50
	v_mov_b32_e32 v98, v50
	v_mov_b32_e32 v99, v50
	v_mov_b32_e32 v100, v50
	v_mov_b32_e32 v101, v50
	v_mov_b32_e32 v102, v50
	v_mov_b32_e32 v103, v50
	v_mov_b32_e32 v104, v50
	v_mov_b32_e32 v105, v50
	v_mov_b32_e32 v82, v50
	v_mov_b32_e32 v83, v50
	v_mov_b32_e32 v84, v50
	v_mov_b32_e32 v85, v50
	v_mov_b32_e32 v86, v50
	v_mov_b32_e32 v87, v50
	v_mov_b32_e32 v88, v50
	v_mov_b32_e32 v89, v50
	v_mov_b32_e32 v54, v50
	v_mov_b32_e32 v55, v50
	v_mov_b32_e32 v56, v50
	v_mov_b32_e32 v57, v50
	v_mov_b32_e32 v62, v50
	v_mov_b32_e32 v63, v50
	v_mov_b32_e32 v64, v50
	v_mov_b32_e32 v65, v50
	v_mov_b32_e32 v58, v50
	v_mov_b32_e32 v59, v50
	v_mov_b32_e32 v60, v50
	v_mov_b32_e32 v61, v50
	v_mov_b32_e32 v70, v50
	v_mov_b32_e32 v71, v50
	v_mov_b32_e32 v72, v50
	v_mov_b32_e32 v73, v50
	v_mov_b32_e32 v42, v50
	v_mov_b32_e32 v43, v50
	v_mov_b32_e32 v44, v50
	v_mov_b32_e32 v45, v50
	v_mov_b32_e32 v46, v50
	v_mov_b32_e32 v47, v50
	v_mov_b32_e32 v48, v50
	v_mov_b32_e32 v49, v50
	v_mov_b32_e32 v66, v50
	v_mov_b32_e32 v67, v50
	v_mov_b32_e32 v68, v50
	v_mov_b32_e32 v69, v50
	v_mov_b32_e32 v74, v50
	v_mov_b32_e32 v75, v50
	v_mov_b32_e32 v76, v50
	v_mov_b32_e32 v77, v50
	v_mov_b32_e32 v150, v50
	v_mov_b32_e32 v151, v50
	v_mov_b32_e32 v240, v156
	v_mov_b32_e32 v241, v157
	v_mov_b32_e32 v246, v158
	v_mov_b32_e32 v247, v159
	v_mov_b32_e32 v242, v164
	v_mov_b32_e32 v243, v165
	v_mov_b32_e32 v244, v166
	v_mov_b32_e32 v245, v167
	s_nop 0
	s_nop 0
	s_nop 0
	s_nop 0
	s_nop 0
	s_nop 0
	s_nop 0
	s_nop 0

; #define ELOADV(kt) do { const char* vb_ = (const char*)Vh + (size_t)(kt) * (64 * LDV * 2); sv0 = *(const bf16x8*)(vb_ + voff0); sv1 = *(const bf16x8*)(vb_ + voff1); sv2 = *(const bf16x8*)(vb_ + voff0 + 256); sv3 = *(const bf16x8*)(vb_ + voff1 + 256); } while (0)
; #define ELOADK(kt) do { const char* kb_ = (const char*)Kh + (size_t)(kt) * (64 * LDK * 2); sk0 = *(const bf16x8*)(kb_ + koff0); sk1 = *(const bf16x8*)(kb_ + koff1); } while (0)
; #define EWRITEV(b) do { char* d_ = V_lds + (b) * D16_V; *(bf16x8*)(d_ + vst0) = sv0; *(bf16x8*)(d_ + vst1) = sv1; *(bf16x8*)(d_ + 8 * VP16 + vst0) = sv2; *(bf16x8*)(d_ + 8 * VP16 + vst1) = sv3; } while (0)
; #define EWRITEK(b) do { char* d_ = K_lds + (b) * PB_K; *(bf16x8*)(d_ + KSWZ(sr, sc * 2)) = sk0; *(bf16x8*)(d_ + KSWZ(32 + sr, sc * 2)) = sk1; } while (0)
; template <int LDQ, int LDK, int LDV, int LDO, int DMX> ...
;     ...
;   { int l16q = l16, gq = g, widq = wid; asm volatile("" : "+v"(l16q), "+v"(gq), "+v"(widq));
;     const bf16* Qw = Qb0 + pass * 128 + (long)((widq & 3) * QBLK + l16q) * LDQ + gq * 8;
; #pragma unroll
;     for (int qt = 0; qt < 2; ++qt)
; #pragma unroll
;       for (int ds = 0; ds < 4; ++ds) qr[qt][ds] = *reinterpret_cast<const bf16x8*>(Qw + (long)qt * 16 * LDQ + ds * 32); }
;   ELOADK(0); ELOADV(0); asm volatile("s_waitcnt vmcnt(0)" ::: "memory"); EWRITEK(0); EWRITEV(0);
;   ELOADK(1); asm volatile("s_waitcnt vmcnt(0)" ::: "memory"); EWRITEK(1); __syncthreads();
.LBB0_1267:
	v_mov_b32_e32 v6, v189
	v_mov_b32_e32 v4, v188
	v_mov_b32_e32 v5, v187
	s_lshl_b64 s[22:23], s[6:7], 1
	s_add_u32 s56, s51, s22
	v_lshlrev_b32_e32 v5, 5, v5
	s_addc_u32 s57, s52, s23
	v_and_b32_e32 v5, 0x60, v5
	v_add_u32_e32 v7, v5, v4
	v_mov_b64_e32 v[4:5], s[56:57]
	v_lshlrev_b32_e32 v6, 3, v6
	v_mad_i64_i32 v[4:5], s[56:57], v7, s28, v[4:5]
	v_ashrrev_i32_e32 v7, 31, v6
	v_lshl_add_u64 v[20:21], v[6:7], 1, v[4:5]
	s_add_u32 s22, s53, s22
	v_add_co_u32_e32 v32, vcc, s26, v20
	s_addc_u32 s23, s54, s23
	s_nop 0
	v_addc_co_u32_e32 v33, vcc, 0, v21, vcc
	v_lshl_add_u64 v[76:77], s[22:23], 0, v[156:157]
	v_add_co_u32_e32 v40, vcc, s29, v76
	global_load_dwordx4 v[4:7], v[20:21], off
	global_load_dwordx4 v[8:11], v[20:21], off offset:64
	global_load_dwordx4 v[12:15], v[20:21], off offset:128
	global_load_dwordx4 v[16:19], v[20:21], off offset:192
	v_addc_co_u32_e32 v41, vcc, 0, v77, vcc
	v_add_co_u32_e32 v60, vcc, s27, v76
	global_load_dwordx4 v[20:23], v[32:33], off
	global_load_dwordx4 v[24:27], v[32:33], off offset:64
	global_load_dwordx4 v[28:31], v[32:33], off offset:128
	s_nop 0
	global_load_dwordx4 v[32:35], v[32:33], off offset:192
	v_addc_co_u32_e32 v61, vcc, 0, v77, vcc
	v_add_co_u32_e32 v64, vcc, s38, v76
	global_load_dwordx4 v[36:39], v[76:77], off
	s_nop 0
	global_load_dwordx4 v[40:43], v[40:41], off
	s_nop 0
	global_load_dwordx4 v[44:47], v[164:165], off
	global_load_dwordx4 v[48:51], v[164:165], off offset:256
	global_load_dwordx4 v[52:55], v[166:167], off
	global_load_dwordx4 v[56:59], v[166:167], off offset:256
	v_addc_co_u32_e32 v65, vcc, 0, v77, vcc
	global_load_dwordx4 v[60:63], v[60:61], off
	s_nop 0
	global_load_dwordx4 v[64:67], v[64:65], off
	v_add_u32_e32 v68, 0, v184
	v_add_u32_e32 v69, 0x10400, v68
	v_add_u32_e32 v68, 0x14800, v68
	s_waitcnt vmcnt(7)
	ds_write_b128 v69, v[36:39]
	s_waitcnt vmcnt(6)
	ds_write_b128 v69, v[40:43] offset:8704
	s_waitcnt vmcnt(5)
	ds_write_b128 v1, v[44:47]
	s_waitcnt vmcnt(3)
	ds_write_b128 v1, v[52:55] offset:1024
	ds_write_b128 v1, v[48:51] offset:16640
	s_waitcnt vmcnt(2)
	ds_write_b128 v1, v[56:59] offset:17664
	s_waitcnt vmcnt(0)
	s_waitcnt vmcnt(1)
	ds_write_b128 v68, v[60:63]
	s_waitcnt vmcnt(0)
	ds_write_b128 v68, v[64:67] offset:8704
	s_waitcnt lgkmcnt(0)
	s_barrier
; template <int LDQ, int LDK, int LDV, int LDO, int DMX> ...
;     ...
;   EQK(0); ESM(0);
;   if (wid >= 4) __builtin_amdgcn_s_setprio(1);
	ds_read_b128 v[36:39], v193
	ds_read_b128 v[40:43], v193 offset:64
	ds_read_b128 v[48:51], v193 offset:4352
	ds_read_b128 v[52:55], v193 offset:4416
	s_waitcnt lgkmcnt(3)
	v_mfma_f32_16x16x32_bf16 v[44:47], v[36:39], v[4:7], 0
	v_mfma_f32_16x16x32_bf16 v[36:39], v[36:39], v[20:23], 0
	s_waitcnt lgkmcnt(1)
	v_mfma_f32_16x16x32_bf16 v[56:59], v[48:51], v[4:7], 0
	v_mfma_f32_16x16x32_bf16 v[48:51], v[48:51], v[20:23], 0
	v_mfma_f32_16x16x32_bf16 v[44:47], v[40:43], v[8:11], v[44:47]
	v_mfma_f32_16x16x32_bf16 v[36:39], v[40:43], v[24:27], v[36:39]
	s_waitcnt lgkmcnt(0)
	v_mfma_f32_16x16x32_bf16 v[40:43], v[52:55], v[8:11], v[56:59]
	v_mfma_f32_16x16x32_bf16 v[48:51], v[52:55], v[24:27], v[48:51]
	ds_read_b128 v[52:55], v193 offset:128
	s_nop 0
	ds_read_b128 v[56:59], v193 offset:192
	s_waitcnt lgkmcnt(1)
	v_mfma_f32_16x16x32_bf16 v[44:47], v[52:55], v[12:15], v[44:47]
	v_mfma_f32_16x16x32_bf16 v[36:39], v[52:55], v[28:31], v[36:39]
	ds_read_b128 v[52:55], v193 offset:4480
	ds_read_b128 v[60:63], v193 offset:4544
	s_waitcnt lgkmcnt(1)
	v_mfma_f32_16x16x32_bf16 v[64:67], v[52:55], v[12:15], v[40:43]
	s_nop 2
	v_add_co_u32_e32 v40, vcc, s39, v76
	v_mfma_f32_16x16x32_bf16 v[68:71], v[52:55], v[28:31], v[48:51]
	s_nop 0
	v_addc_co_u32_e32 v41, vcc, 0, v77, vcc
	v_add_co_u32_e32 v42, vcc, s40, v76
	v_mfma_f32_16x16x32_bf16 v[72:75], v[56:59], v[16:19], v[44:47]
	s_nop 0
	v_addc_co_u32_e32 v43, vcc, 0, v77, vcc
	v_mfma_f32_16x16x32_bf16 v[76:79], v[56:59], v[32:35], v[36:39]
	global_load_dwordx4 v[52:55], v[40:41], off
	global_load_dwordx4 v[56:59], v[42:43], off
	s_nop 0
	s_waitcnt lgkmcnt(0)
	v_mfma_f32_16x16x32_bf16 v[64:67], v[60:63], v[16:19], v[64:67]
	v_mfma_f32_16x16x32_bf16 v[68:71], v[60:63], v[32:35], v[68:71]
	v_add_f32_e32 v61, v200, v73
	v_exp_f32_e32 v62, v61
	v_add_f32_e32 v61, v200, v74
	v_add_f32_e32 v60, v200, v72
	v_exp_f32_e32 v72, v61
	v_add_f32_e32 v61, v200, v75
	s_nop 0
	v_add_f32_e32 v64, v200, v64
	v_exp_f32_e32 v74, v61
	v_add_f32_e32 v61, v200, v76
	v_exp_f32_e32 v76, v64
	v_add_f32_e32 v64, v200, v65
	v_add_f32_e32 v73, v200, v78
	v_exp_f32_e32 v78, v64
	v_add_f32_e32 v64, v200, v66
	v_exp_f32_e32 v80, v64
	v_add_f32_e32 v64, v200, v67
	v_exp_f32_e32 v82, v64
	v_add_f32_e32 v64, v200, v68
	v_add_f32_e32 v63, v200, v77
	v_exp_f32_e32 v77, v64
	v_add_f32_e32 v64, v200, v69
	v_add_f32_e32 v75, v200, v79
	v_exp_f32_e32 v79, v64
	v_add_f32_e32 v64, v200, v70
	v_exp_f32_e32 v81, v64
	v_add_f32_e32 v64, v200, v71
	v_exp_f32_e32 v60, v60
	v_exp_f32_e32 v61, v61
	v_exp_f32_e32 v63, v63
	v_exp_f32_e32 v73, v73
	v_exp_f32_e32 v75, v75
	v_exp_f32_e32 v83, v64
	v_cvt_pk_bf16_f32 v64, v60, v62
	v_cvt_pk_bf16_f32 v65, v72, v74
	v_cvt_pk_bf16_f32 v66, v76, v78
	v_cvt_pk_bf16_f32 v67, v80, v82
	v_cvt_pk_bf16_f32 v68, v61, v63
	v_cvt_pk_bf16_f32 v69, v73, v75
	v_cvt_pk_bf16_f32 v70, v77, v79
	v_cvt_pk_bf16_f32 v71, v81, v83
	ds_write_b128 v190, v[64:67]
	ds_write_b128 v190, v[68:71] offset:1024
	s_and_saveexec_b64 s[22:23], s[4:5]
	s_setprio 1
	s_or_b64 exec, exec, s[22:23]
	v_pk_add_f32 v[60:61], v[60:61], v[62:63]
	v_pk_add_f32 v[62:63], v[72:73], v[74:75]
	v_pk_add_f32 v[72:73], v[80:81], v[82:83]
	v_pk_add_f32 v[60:61], v[60:61], v[62:63]
	v_pk_add_f32 v[62:63], v[76:77], v[78:79]
	v_mov_b32_e32 v112, 0
	v_pk_add_f32 v[62:63], v[62:63], v[72:73]
	s_xor_b64 s[20:21], s[20:21], -1
	v_pk_add_f32 v[60:61], v[60:61], v[62:63]
	s_mov_b32 s55, 1
	v_pk_add_f32 v[174:175], v[60:61], 0 op_sel_hi:[1,0]
	s_add_u32 s74, s72, 0xc0000
	s_addc_u32 s75, s73, 0
	s_add_u32 s76, s74, 0x60000
	s_addc_u32 s77, s75, 0
	v_lshl_add_u64 v[176:177], s[6:7], 1, v[172:173]
	s_mov_b64 s[6:7], 0
	s_movk_i32 s56, 0x4000
	v_mov_b32_e32 v113, v112
	v_mov_b32_e32 v114, v112
	v_mov_b32_e32 v115, v112
	v_mov_b32_e32 v120, v112
	v_mov_b32_e32 v121, v112
	v_mov_b32_e32 v122, v112
	v_mov_b32_e32 v123, v112
	v_mov_b32_e32 v124, v112
	v_mov_b32_e32 v125, v112
	v_mov_b32_e32 v126, v112
	v_mov_b32_e32 v127, v112
	v_mov_b32_e32 v128, v112
	v_mov_b32_e32 v129, v112
	v_mov_b32_e32 v130, v112
	v_mov_b32_e32 v131, v112
	v_mov_b32_e32 v108, v112
	v_mov_b32_e32 v109, v112
	v_mov_b32_e32 v110, v112
	v_mov_b32_e32 v111, v112
	v_mov_b32_e32 v116, v112
	v_mov_b32_e32 v117, v112
	v_mov_b32_e32 v118, v112
	v_mov_b32_e32 v119, v112
	v_mov_b32_e32 v100, v112
	v_mov_b32_e32 v101, v112
	v_mov_b32_e32 v102, v112
	v_mov_b32_e32 v103, v112
	v_mov_b32_e32 v104, v112
	v_mov_b32_e32 v105, v112
	v_mov_b32_e32 v106, v112
	v_mov_b32_e32 v107, v112
	v_mov_b32_e32 v84, v112
	v_mov_b32_e32 v85, v112
	v_mov_b32_e32 v86, v112
	v_mov_b32_e32 v87, v112
	v_mov_b32_e32 v92, v112
	v_mov_b32_e32 v93, v112
	v_mov_b32_e32 v94, v112
	v_mov_b32_e32 v95, v112
	v_mov_b32_e32 v88, v112
	v_mov_b32_e32 v89, v112
	v_mov_b32_e32 v90, v112
	v_mov_b32_e32 v91, v112
	v_mov_b32_e32 v96, v112
	v_mov_b32_e32 v97, v112
	v_mov_b32_e32 v98, v112
	v_mov_b32_e32 v99, v112
	v_mov_b32_e32 v60, v112
	v_mov_b32_e32 v61, v112
	v_mov_b32_e32 v62, v112
	v_mov_b32_e32 v63, v112
	v_mov_b32_e32 v80, v112
	v_mov_b32_e32 v81, v112
	v_mov_b32_e32 v82, v112
	v_mov_b32_e32 v83, v112
	v_mov_b32_e32 v72, v112
	v_mov_b32_e32 v73, v112
	v_mov_b32_e32 v74, v112
	v_mov_b32_e32 v75, v112
	v_mov_b32_e32 v76, v112
	v_mov_b32_e32 v77, v112
	v_mov_b32_e32 v78, v112
	v_mov_b32_e32 v79, v112
	s_branch .Lvd_entry
.Lvd_entry:
	s_add_i32 s60, s55, -1
	s_and_b32 s57, s60, 1
	s_bitcmp1_b32 s55, 0
	s_cselect_b64 s[22:23], -1, 0
	s_and_b64 s[58:59], s[22:23], exec
	s_cselect_b32 s58, 0x4400, 0
	s_cselect_b32 s85, 0x8200, 0
	s_add_i32 s85, s85, s84
	v_add_u32_e32 v178, s58, v193
	s_nop 0
	s_nop 0
	s_nop 0
	s_nop 0
	s_nop 0
	s_nop 0
